# P1 RoPE epilogue: per-lane sin sign by one +-1.0 select and two packed multiplies instead of 4 xor + 4 cndmask (10 of 16 blocks)
# speedup vs baseline: 1.0068x; 1.0068x over previous
.LBB0_135:
	s_lshl_b32 s8, s49, 10
	s_and_b32 s8, s8, 0x400
	s_add_i32 s8, s8, 0
	s_add_i32 s8, s8, 0x24cc0
	v_lshlrev_b32_e32 v138, 2, v201
	v_lshlrev_b32_e32 v139, 2, v200
	v_add3_u32 v226, s8, v138, v139
	ds_read_b32 v200, v226
	v_cndmask_b32_e64 v138, 0, 1, s[54:55]
	v_cmp_eq_u32_e64 s[8:9], 0, v228
	v_cmp_ne_u32_e64 s[10:11], 1, v138
	s_andn2_b64 vcc, exec, s[54:55]
	s_waitcnt lgkmcnt(0)
	v_pk_mul_f32 v[192:193], v[192:193], v[200:201] op_sel_hi:[1,0]
	v_pk_mul_f32 v[190:191], v[190:191], v[200:201] op_sel_hi:[1,0]
	v_pk_mul_f32 v[188:189], v[188:189], v[200:201] op_sel_hi:[1,0]
	v_pk_mul_f32 v[202:203], v[186:187], v[200:201] op_sel_hi:[1,0]
	s_cbranch_vccnz .LBB0_139
	v_and_b32_e32 v139, 64, v225
	v_xor_b32_e32 v138, 16, v225
	v_add_u32_e32 v139, 64, v139
	v_cmp_lt_i32_e32 vcc, v138, v139
	s_nop 1
	v_cndmask_b32_e32 v138, v225, v138, vcc
	v_lshlrev_b32_e32 v138, 2, v138
	ds_bpermute_b32 v208, v138, v190
	ds_bpermute_b32 v204, v138, v202
	ds_bpermute_b32 v209, v138, v191
	ds_bpermute_b32 v205, v138, v203
	ds_bpermute_b32 v206, v138, v192
	ds_bpermute_b32 v186, v138, v188
	ds_bpermute_b32 v207, v138, v193
	ds_bpermute_b32 v187, v138, v189
	s_and_saveexec_b64 s[54:55], s[6:7]
	s_cbranch_execz .LBB0_138
	v_cndmask_b32_e64 v140, 1.0, -1.0, s[8:9]
	v_pk_mul_f32 v[138:139], v[128:129], v[140:141] op_sel_hi:[1,0]
	v_pk_mul_f32 v[140:141], v[126:127], v[140:141] op_sel_hi:[1,0]
	s_waitcnt lgkmcnt(5)
	v_pk_mul_f32 v[140:141], v[140:141], v[208:209]
	s_waitcnt lgkmcnt(1)
	v_pk_mul_f32 v[138:139], v[138:139], v[206:207]
	v_pk_fma_f32 v[190:191], v[122:123], v[190:191], v[140:141]
	v_pk_fma_f32 v[192:193], v[124:125], v[192:193], v[138:139]
	v_cndmask_b32_e64 v140, 1.0, -1.0, s[8:9]
	v_pk_mul_f32 v[138:139], v[120:121], v[140:141] op_sel_hi:[1,0]
	v_pk_mul_f32 v[140:141], v[118:119], v[140:141] op_sel_hi:[1,0]
	v_pk_mul_f32 v[140:141], v[140:141], v[204:205]
	s_waitcnt lgkmcnt(0)
	v_pk_mul_f32 v[138:139], v[138:139], v[186:187]
	v_pk_fma_f32 v[202:203], v[114:115], v[202:203], v[140:141]
	v_pk_fma_f32 v[188:189], v[116:117], v[188:189], v[138:139]

.LBB0_139:
	v_and_b32_e32 v138, 0xc0, v227
	v_lshl_or_b32 v138, s52, 8, v138
	v_mov_b32_e32 v201, v200
	s_waitcnt lgkmcnt(2)
	v_lshl_or_b32 v186, v228, 3, v138
	v_mov_b32_e32 v138, v200
	v_mov_b32_e32 v139, v200
	v_pk_mul_f32 v[144:145], v[184:185], v[138:139]
	v_pk_mul_f32 v[142:143], v[182:183], v[200:201]
	v_pk_mul_f32 v[178:179], v[178:179], v[200:201]
	v_pk_mul_f32 v[180:181], v[180:181], v[138:139]
	v_cvt_pk_bf16_f32 v138, v190, v191
	v_cvt_pk_bf16_f32 v139, v192, v193
	v_cvt_pk_bf16_f32 v140, v202, v203
	v_cvt_pk_bf16_f32 v141, v188, v189
	v_cvt_pk_bf16_f32 v142, v142, v143
	v_cvt_pk_bf16_f32 v143, v144, v145
	v_cvt_pk_bf16_f32 v144, v178, v179
	s_nop 0
	v_cvt_pk_bf16_f32 v145, v180, v181
	ds_read_b32 v178, v226 offset:64
	v_ashrrev_i32_e32 v199, 31, v198
	v_lshlrev_b64 v[204:205], 12, v[198:199]
	s_waitcnt lgkmcnt(1)
	v_ashrrev_i32_e32 v187, 31, v186
	v_lshl_add_u64 v[180:181], s[18:19], 0, v[204:205]
	v_lshl_add_u64 v[180:181], v[186:187], 1, v[180:181]
	s_waitcnt lgkmcnt(0)
	v_pk_mul_f32 v[176:177], v[176:177], v[178:179] op_sel_hi:[1,0]
	v_pk_mul_f32 v[174:175], v[174:175], v[178:179] op_sel_hi:[1,0]
	v_pk_mul_f32 v[172:173], v[172:173], v[178:179] op_sel_hi:[1,0]
	s_and_b64 vcc, exec, s[10:11]
	v_pk_mul_f32 v[170:171], v[170:171], v[178:179] op_sel_hi:[1,0]
	global_store_dwordx4 v[180:181], v[138:141], off
	global_store_dwordx4 v[180:181], v[142:145], off offset:64
	s_cbranch_vccnz .LBB0_143
	v_and_b32_e32 v139, 64, v225
	v_xor_b32_e32 v138, 16, v225
	v_add_u32_e32 v139, 64, v139
	v_cmp_lt_i32_e32 vcc, v138, v139
	s_nop 1
	v_cndmask_b32_e32 v138, v225, v138, vcc
	v_lshlrev_b32_e32 v138, 2, v138
	ds_bpermute_b32 v188, v138, v174
	ds_bpermute_b32 v182, v138, v170
	ds_bpermute_b32 v189, v138, v175
	ds_bpermute_b32 v183, v138, v171
	ds_bpermute_b32 v184, v138, v176
	ds_bpermute_b32 v180, v138, v172
	ds_bpermute_b32 v185, v138, v177
	ds_bpermute_b32 v181, v138, v173
	s_and_saveexec_b64 s[52:53], s[6:7]
	s_cbranch_execz .LBB0_142
	v_cndmask_b32_e64 v140, 1.0, -1.0, s[8:9]
	v_pk_mul_f32 v[138:139], v[96:97], v[140:141] op_sel_hi:[1,0]
	v_pk_mul_f32 v[140:141], v[94:95], v[140:141] op_sel_hi:[1,0]
	s_waitcnt lgkmcnt(5)
	v_pk_mul_f32 v[140:141], v[140:141], v[188:189]
	s_waitcnt lgkmcnt(1)
	v_pk_mul_f32 v[138:139], v[138:139], v[184:185]
	v_pk_fma_f32 v[174:175], v[230:231], v[174:175], v[140:141]
	v_pk_fma_f32 v[176:177], v[232:233], v[176:177], v[138:139]
	v_cndmask_b32_e64 v140, 1.0, -1.0, s[8:9]
	v_pk_mul_f32 v[138:139], v[88:89], v[140:141] op_sel_hi:[1,0]
	v_pk_mul_f32 v[140:141], v[86:87], v[140:141] op_sel_hi:[1,0]
	v_pk_mul_f32 v[140:141], v[140:141], v[182:183]
	s_waitcnt lgkmcnt(0)
	v_pk_mul_f32 v[138:139], v[138:139], v[180:181]
	v_pk_fma_f32 v[170:171], v[194:195], v[170:171], v[140:141]
	v_pk_fma_f32 v[172:173], v[196:197], v[172:173], v[138:139]

.LBB0_143:
	v_or_b32_e32 v138, 16, v198
	v_ashrrev_i32_e32 v139, 31, v138
	v_mov_b32_e32 v179, v178
	s_waitcnt lgkmcnt(0)
	v_lshlrev_b64 v[180:181], 12, v[138:139]
	v_mov_b32_e32 v138, v178
	v_mov_b32_e32 v139, v178
	v_pk_mul_f32 v[144:145], v[168:169], v[138:139]
	v_pk_mul_f32 v[142:143], v[166:167], v[178:179]
	v_pk_mul_f32 v[162:163], v[162:163], v[178:179]
	v_pk_mul_f32 v[164:165], v[164:165], v[138:139]
	v_cvt_pk_bf16_f32 v138, v174, v175
	v_cvt_pk_bf16_f32 v139, v176, v177
	v_cvt_pk_bf16_f32 v140, v170, v171
	v_cvt_pk_bf16_f32 v141, v172, v173
	v_cvt_pk_bf16_f32 v142, v142, v143
	v_cvt_pk_bf16_f32 v143, v144, v145
	v_cvt_pk_bf16_f32 v144, v162, v163
	s_nop 0
	v_cvt_pk_bf16_f32 v145, v164, v165
	ds_read_b32 v162, v226 offset:128
	v_lshl_add_u64 v[164:165], s[18:19], 0, v[180:181]
	v_lshl_add_u64 v[164:165], v[186:187], 1, v[164:165]
	s_and_b64 vcc, exec, s[10:11]
	global_store_dwordx4 v[164:165], v[138:141], off
	global_store_dwordx4 v[164:165], v[142:145], off offset:64
	s_waitcnt lgkmcnt(0)
	v_pk_mul_f32 v[160:161], v[160:161], v[162:163] op_sel_hi:[1,0]
	v_pk_mul_f32 v[158:159], v[158:159], v[162:163] op_sel_hi:[1,0]
	v_pk_mul_f32 v[156:157], v[156:157], v[162:163] op_sel_hi:[1,0]
	v_pk_mul_f32 v[154:155], v[154:155], v[162:163] op_sel_hi:[1,0]
	s_cbranch_vccnz .LBB0_147
	v_and_b32_e32 v139, 64, v225
	v_xor_b32_e32 v138, 16, v225
	v_add_u32_e32 v139, 64, v139
	v_cmp_lt_i32_e32 vcc, v138, v139
	s_nop 1
	v_cndmask_b32_e32 v138, v225, v138, vcc
	v_lshlrev_b32_e32 v138, 2, v138
	ds_bpermute_b32 v170, v138, v158
	ds_bpermute_b32 v166, v138, v154
	ds_bpermute_b32 v171, v138, v159
	ds_bpermute_b32 v167, v138, v155
	ds_bpermute_b32 v168, v138, v160
	ds_bpermute_b32 v164, v138, v156
	ds_bpermute_b32 v169, v138, v161
	ds_bpermute_b32 v165, v138, v157
	s_and_saveexec_b64 s[52:53], s[6:7]
	s_cbranch_execz .LBB0_146
	v_cndmask_b32_e64 v140, 1.0, -1.0, s[8:9]
	v_pk_mul_f32 v[138:139], v[72:73], v[140:141] op_sel_hi:[1,0]
	v_pk_mul_f32 v[140:141], v[70:71], v[140:141] op_sel_hi:[1,0]
	s_waitcnt lgkmcnt(5)
	v_pk_mul_f32 v[140:141], v[140:141], v[170:171]
	s_waitcnt lgkmcnt(1)
	v_pk_mul_f32 v[138:139], v[138:139], v[168:169]
	v_pk_fma_f32 v[158:159], v[62:63], v[158:159], v[140:141]
	v_pk_fma_f32 v[160:161], v[64:65], v[160:161], v[138:139]
	v_cndmask_b32_e64 v140, 1.0, -1.0, s[8:9]
	v_pk_mul_f32 v[138:139], v[68:69], v[140:141] op_sel_hi:[1,0]
	v_pk_mul_f32 v[140:141], v[66:67], v[140:141] op_sel_hi:[1,0]
	v_pk_mul_f32 v[140:141], v[140:141], v[166:167]
	s_waitcnt lgkmcnt(0)
	v_pk_mul_f32 v[138:139], v[138:139], v[164:165]
	v_pk_fma_f32 v[154:155], v[58:59], v[154:155], v[140:141]
	v_pk_fma_f32 v[156:157], v[60:61], v[156:157], v[138:139]

.LBB0_147:
	v_or_b32_e32 v138, 32, v198
	v_ashrrev_i32_e32 v139, 31, v138
	v_mov_b32_e32 v163, v162
	s_waitcnt lgkmcnt(0)
	v_lshlrev_b64 v[164:165], 12, v[138:139]
	v_mov_b32_e32 v138, v162
	v_mov_b32_e32 v139, v162
	v_pk_mul_f32 v[144:145], v[152:153], v[138:139]
	v_pk_mul_f32 v[142:143], v[150:151], v[162:163]
	v_pk_mul_f32 v[146:147], v[146:147], v[162:163]
	v_pk_mul_f32 v[148:149], v[148:149], v[138:139]
	v_cvt_pk_bf16_f32 v138, v158, v159
	v_cvt_pk_bf16_f32 v139, v160, v161
	v_cvt_pk_bf16_f32 v140, v154, v155
	v_cvt_pk_bf16_f32 v141, v156, v157
	v_cvt_pk_bf16_f32 v142, v142, v143
	v_cvt_pk_bf16_f32 v143, v144, v145
	v_cvt_pk_bf16_f32 v144, v146, v147
	s_nop 0
	v_cvt_pk_bf16_f32 v145, v148, v149
	ds_read_b32 v146, v226 offset:192
	v_lshl_add_u64 v[148:149], s[18:19], 0, v[164:165]
	v_lshl_add_u64 v[148:149], v[186:187], 1, v[148:149]
	global_store_dwordx4 v[148:149], v[138:141], off
	global_store_dwordx4 v[148:149], v[142:145], off offset:64
	s_and_b64 vcc, exec, s[10:11]
	s_waitcnt lgkmcnt(0)
	v_pk_mul_f32 v[140:141], v[100:101], v[146:147] op_sel_hi:[1,0]
	v_pk_mul_f32 v[144:145], v[104:105], v[146:147] op_sel_hi:[1,0]
	v_pk_mul_f32 v[142:143], v[102:103], v[146:147] op_sel_hi:[1,0]
	v_pk_mul_f32 v[138:139], v[98:99], v[146:147] op_sel_hi:[1,0]
	s_cbranch_vccnz .LBB0_151
	v_and_b32_e32 v99, 64, v225
	v_xor_b32_e32 v98, 16, v225
	v_add_u32_e32 v99, 64, v99
	v_cmp_lt_i32_e32 vcc, v98, v99
	s_nop 1
	v_cndmask_b32_e32 v98, v225, v98, vcc
	v_lshlrev_b32_e32 v98, 2, v98
	ds_bpermute_b32 v154, v98, v142
	ds_bpermute_b32 v150, v98, v138
	ds_bpermute_b32 v155, v98, v143
	ds_bpermute_b32 v151, v98, v139
	ds_bpermute_b32 v152, v98, v144
	ds_bpermute_b32 v148, v98, v140
	ds_bpermute_b32 v153, v98, v145
	ds_bpermute_b32 v149, v98, v141
	s_and_saveexec_b64 s[52:53], s[6:7]
	s_cbranch_execz .LBB0_150
	v_cndmask_b32_e64 v100, 1.0, -1.0, s[8:9]
	v_pk_mul_f32 v[98:99], v[48:49], v[100:101] op_sel_hi:[1,0]
	v_pk_mul_f32 v[100:101], v[46:47], v[100:101] op_sel_hi:[1,0]
	s_waitcnt lgkmcnt(5)
	v_pk_mul_f32 v[100:101], v[100:101], v[154:155]
	s_waitcnt lgkmcnt(1)
	v_pk_mul_f32 v[98:99], v[98:99], v[152:153]
	v_pk_fma_f32 v[142:143], v[42:43], v[142:143], v[100:101]
	v_pk_fma_f32 v[144:145], v[44:45], v[144:145], v[98:99]
	v_cndmask_b32_e64 v100, 1.0, -1.0, s[8:9]
	v_pk_mul_f32 v[98:99], v[36:37], v[100:101] op_sel_hi:[1,0]
	v_pk_mul_f32 v[100:101], v[34:35], v[100:101] op_sel_hi:[1,0]
	v_pk_mul_f32 v[100:101], v[100:101], v[150:151]
	s_waitcnt lgkmcnt(0)
	v_pk_mul_f32 v[98:99], v[98:99], v[148:149]
	v_pk_fma_f32 v[138:139], v[26:27], v[138:139], v[100:101]
	v_pk_fma_f32 v[140:141], v[28:29], v[140:141], v[98:99]

.LBB0_155:
	ds_read_b32 v130, v226 offset:512
	s_and_b64 vcc, exec, s[10:11]
	s_waitcnt lgkmcnt(0)
	v_pk_mul_f32 v[132:133], v[108:109], v[130:131] op_sel_hi:[1,0]
	v_pk_mul_f32 v[134:135], v[106:107], v[130:131] op_sel_hi:[1,0]
	v_pk_mul_f32 v[108:109], v[112:113], v[130:131] op_sel_hi:[1,0]
	v_pk_mul_f32 v[110:111], v[110:111], v[130:131] op_sel_hi:[1,0]
	s_cbranch_vccnz .LBB0_159
	v_and_b32_e32 v99, 64, v225
	v_xor_b32_e32 v98, 16, v225
	v_add_u32_e32 v99, 64, v99
	v_cmp_lt_i32_e32 vcc, v98, v99
	s_nop 1
	v_cndmask_b32_e32 v98, v225, v98, vcc
	v_lshlrev_b32_e32 v98, 2, v98
	ds_bpermute_b32 v138, v98, v134
	ds_bpermute_b32 v112, v98, v110
	ds_bpermute_b32 v139, v98, v135
	ds_bpermute_b32 v113, v98, v111
	ds_bpermute_b32 v136, v98, v132
	ds_bpermute_b32 v106, v98, v108
	ds_bpermute_b32 v137, v98, v133
	ds_bpermute_b32 v107, v98, v109
	s_and_saveexec_b64 s[52:53], s[6:7]
	s_cbranch_execz .LBB0_158
	v_cndmask_b32_e64 v100, 1.0, -1.0, s[8:9]
	v_pk_mul_f32 v[98:99], v[128:129], v[100:101] op_sel_hi:[1,0]
	v_pk_mul_f32 v[100:101], v[126:127], v[100:101] op_sel_hi:[1,0]
	s_waitcnt lgkmcnt(5)
	v_pk_mul_f32 v[100:101], v[100:101], v[138:139]
	s_waitcnt lgkmcnt(1)
	v_pk_mul_f32 v[98:99], v[98:99], v[136:137]
	v_pk_fma_f32 v[134:135], v[122:123], v[134:135], v[100:101]
	v_pk_fma_f32 v[132:133], v[124:125], v[132:133], v[98:99]
	v_cndmask_b32_e64 v100, 1.0, -1.0, s[8:9]
	v_pk_mul_f32 v[98:99], v[120:121], v[100:101] op_sel_hi:[1,0]
	v_pk_mul_f32 v[100:101], v[118:119], v[100:101] op_sel_hi:[1,0]
	v_pk_mul_f32 v[100:101], v[100:101], v[112:113]
	s_waitcnt lgkmcnt(0)
	v_pk_mul_f32 v[98:99], v[98:99], v[106:107]
	v_pk_fma_f32 v[110:111], v[114:115], v[110:111], v[100:101]
	v_pk_fma_f32 v[108:109], v[116:117], v[108:109], v[98:99]
